# v46 + MLA loop: the packed v_pk_fma_f32 of the next-half score scaling split into scalar v_fma_f32 pairs
# speedup vs baseline: 1.0057x; 1.0057x over previous
.LBB0_565:
	s_waitcnt lgkmcnt(4)
	v_mfma_scale_f32_32x32x64_f8f6f4 v[96:111], v[96:103], v[120:127], 0, v205, v205 op_sel_hi:[0,0,0]
	v_cndmask_b32_e64 v176, v189, v192, s[4:5]
	v_fma_f32 v80, v80, s40, -v176
	v_fma_f32 v81, v81, s40, -v176
	v_fma_f32 v84, v84, s40, -v176
	v_fma_f32 v85, v85, s40, -v176
	v_fma_f32 v88, v88, s40, -v176
	v_fma_f32 v89, v89, s40, -v176
	v_fma_f32 v92, v92, s40, -v176
	v_fma_f32 v93, v93, s40, -v176
	v_exp_f32_e32 v80, v80
	v_exp_f32_e32 v81, v81
	v_exp_f32_e32 v84, v84
	v_exp_f32_e32 v85, v85
	v_exp_f32_e32 v88, v88
	v_exp_f32_e32 v89, v89
	s_waitcnt lgkmcnt(2)
	v_mfma_scale_f32_32x32x64_f8f6f4 v[96:111], v[156:163], v[128:135], v[96:111], v205, v205 op_sel_hi:[0,0,0]
	v_exp_f32_e32 v92, v92
	v_exp_f32_e32 v93, v93
	v_fma_f32 v82, v82, s40, -v176
	v_fma_f32 v83, v83, s40, -v176
	v_fma_f32 v86, v86, s40, -v176
	v_fma_f32 v87, v87, s40, -v176
	v_fma_f32 v90, v90, s40, -v176
	v_fma_f32 v91, v91, s40, -v176
	v_fma_f32 v94, v94, s40, -v176
	v_fma_f32 v95, v95, s40, -v176
	v_exp_f32_e32 v82, v82
	v_exp_f32_e32 v83, v83
	v_exp_f32_e32 v86, v86
	v_exp_f32_e32 v87, v87
	v_exp_f32_e32 v90, v90
	s_waitcnt lgkmcnt(0)
	v_mfma_scale_f32_32x32x64_f8f6f4 v[96:111], v[148:155], v[136:143], v[96:111], v205, v205 op_sel_hi:[0,0,0]
	v_lshl_add_u32 v240, s23, 14, v211
	ds_read_b128 v[224:227], v240
	ds_read_b128 v[228:231], v240 offset:16
	ds_read_b128 v[232:235], v240 offset:2560
	ds_read_b128 v[236:239], v240 offset:2576
	v_exp_f32_e32 v91, v91
	v_exp_f32_e32 v94, v94
	v_exp_f32_e32 v95, v95
	v_cvt_pk_fp8_f32 v148, v80, v81
	v_cvt_pk_fp8_f32 v149, v84, v85
	v_cvt_pk_fp8_f32 v150, v88, v89
	v_cvt_pk_fp8_f32 v151, v92, v93
	v_cvt_pk_fp8_f32 v148, v82, v83 op_sel:[0,0,1]
	v_cvt_pk_fp8_f32 v149, v86, v87 op_sel:[0,0,1]
	v_cvt_pk_fp8_f32 v150, v90, v91 op_sel:[0,0,1]
	v_cvt_pk_fp8_f32 v151, v94, v95 op_sel:[0,0,1]
	s_nop 0
	s_waitcnt lgkmcnt(2)
	v_mfma_scale_f32_32x32x64_f8f6f4 v[48:63], v[144:151], v[224:231], v[48:63], v205, v205 op_sel_hi:[0,0,0]
	ds_read_b128 v[80:83], v240 offset:5120
	ds_read_b128 v[84:87], v240 offset:5136
	ds_read_b128 v[152:155], v240 offset:7680
	ds_read_b128 v[156:159], v240 offset:7696
	s_waitcnt lgkmcnt(4)
	v_mfma_scale_f32_32x32x64_f8f6f4 v[32:47], v[144:151], v[232:239], v[32:47], v205, v205 op_sel_hi:[0,0,0]
	v_max_f32_e32 v88, v96, v97
	v_max3_f32 v88, v88, v98, v99
	v_max3_f32 v88, v88, v100, v101
	v_max3_f32 v88, v88, v102, v103
	v_max3_f32 v88, v88, v104, v105
	v_max3_f32 v88, v88, v106, v107
	s_waitcnt lgkmcnt(2)
	v_mfma_scale_f32_32x32x64_f8f6f4 v[16:31], v[144:151], v[80:87], v[16:31], v205, v205 op_sel_hi:[0,0,0]
	v_max3_f32 v88, v88, v108, v109
	v_max3_f32 v88, v88, v110, v111
	v_mov_b32_e32 v89, v88
	s_nop 1
	v_permlane32_swap_b32_e32 v88, v89
	v_max_f32_e32 v80, v88, v89
	v_fma_f32 v81, v80, s40, -v176
	v_cmp_ge_f32_e32 vcc, s70, v81
	v_fmamk_f32 v80, v80, 0x3dd53b94, v202
	v_max_f32_e32 v80, v176, v80
	v_sub_f32_e32 v81, v176, v80
	v_exp_f32_e32 v81, v81
	s_waitcnt lgkmcnt(0)
	v_mfma_scale_f32_32x32x64_f8f6f4 v[0:15], v[144:151], v[152:159], v[0:15], v205, v205 op_sel_hi:[0,0,0]
	s_cmp_eq_u64 vcc, exec
	s_cselect_b64 vcc, -1, 0
	v_cndmask_b32_e32 v192, v80, v176, vcc
	s_add_i32 s21, s21, 2
	s_add_i32 s78, s78, 1
	s_add_i32 s22, s22, 64
	v_fma_f32 v178, v96, s40, -v192
	v_fma_f32 v179, v97, s40, -v192
	v_fma_f32 v176, v98, s40, -v192
	v_fma_f32 v177, v99, s40, -v192
	v_fma_f32 v162, v100, s40, -v192
	v_fma_f32 v163, v101, s40, -v192
	v_fma_f32 v160, v102, s40, -v192
	v_fma_f32 v161, v103, s40, -v192
	v_fma_f32 v158, v104, s40, -v192
	v_fma_f32 v159, v105, s40, -v192
	v_fma_f32 v156, v106, s40, -v192
	v_fma_f32 v157, v107, s40, -v192
	v_fma_f32 v154, v108, s40, -v192
	v_fma_f32 v155, v109, s40, -v192
	v_fma_f32 v152, v110, s40, -v192
	v_fma_f32 v153, v111, s40, -v192
	v_cndmask_b32_e64 v88, v81, 1.0, vcc
	v_mfma_scale_f32_32x32x64_f8f6f4 v[64:79], v[144:151], v[112:119], v[64:79], v205, v205 op_sel_hi:[0,0,0]
	s_cmp_ge_u32 s21, s17
	s_barrier
	s_cbranch_scc1 .LBB0_580

.LBB0_1875:
	s_waitcnt lgkmcnt(4)
	v_mfma_scale_f32_32x32x64_f8f6f4 v[96:111], v[96:103], v[120:127], 0, v207, v207 op_sel_hi:[0,0,0]
	v_cndmask_b32_e64 v176, v191, v194, s[4:5]
	v_fma_f32 v80, v80, s38, -v176
	v_fma_f32 v81, v81, s38, -v176
	v_fma_f32 v84, v84, s38, -v176
	v_fma_f32 v85, v85, s38, -v176
	v_fma_f32 v88, v88, s38, -v176
	v_fma_f32 v89, v89, s38, -v176
	v_fma_f32 v92, v92, s38, -v176
	v_fma_f32 v93, v93, s38, -v176
	v_exp_f32_e32 v80, v80
	v_exp_f32_e32 v81, v81
	v_exp_f32_e32 v84, v84
	v_exp_f32_e32 v85, v85
	v_exp_f32_e32 v88, v88
	v_exp_f32_e32 v89, v89
	s_waitcnt lgkmcnt(2)
	v_mfma_scale_f32_32x32x64_f8f6f4 v[96:111], v[156:163], v[128:135], v[96:111], v207, v207 op_sel_hi:[0,0,0]
	v_exp_f32_e32 v92, v92
	v_exp_f32_e32 v93, v93
	v_fma_f32 v82, v82, s38, -v176
	v_fma_f32 v83, v83, s38, -v176
	v_fma_f32 v86, v86, s38, -v176
	v_fma_f32 v87, v87, s38, -v176
	v_fma_f32 v90, v90, s38, -v176
	v_fma_f32 v91, v91, s38, -v176
	v_fma_f32 v94, v94, s38, -v176
	v_fma_f32 v95, v95, s38, -v176
	v_exp_f32_e32 v82, v82
	v_exp_f32_e32 v83, v83
	v_exp_f32_e32 v86, v86
	v_exp_f32_e32 v87, v87
	v_exp_f32_e32 v90, v90
	s_waitcnt lgkmcnt(0)
	v_mfma_scale_f32_32x32x64_f8f6f4 v[96:111], v[148:155], v[136:143], v[96:111], v207, v207 op_sel_hi:[0,0,0]
	v_lshl_add_u32 v240, s24, 14, v209
	ds_read_b128 v[224:227], v240
	ds_read_b128 v[228:231], v240 offset:16
	ds_read_b128 v[232:235], v240 offset:2560
	ds_read_b128 v[236:239], v240 offset:2576
	v_exp_f32_e32 v91, v91
	v_exp_f32_e32 v94, v94
	v_exp_f32_e32 v95, v95
	v_cvt_pk_fp8_f32 v148, v80, v81
	v_cvt_pk_fp8_f32 v149, v84, v85
	v_cvt_pk_fp8_f32 v150, v88, v89
	v_cvt_pk_fp8_f32 v151, v92, v93
	v_cvt_pk_fp8_f32 v148, v82, v83 op_sel:[0,0,1]
	v_cvt_pk_fp8_f32 v149, v86, v87 op_sel:[0,0,1]
	v_cvt_pk_fp8_f32 v150, v90, v91 op_sel:[0,0,1]
	v_cvt_pk_fp8_f32 v151, v94, v95 op_sel:[0,0,1]
	s_nop 0
	s_waitcnt lgkmcnt(2)
	v_mfma_scale_f32_32x32x64_f8f6f4 v[48:63], v[144:151], v[224:231], v[48:63], v207, v207 op_sel_hi:[0,0,0]
	ds_read_b128 v[80:83], v240 offset:5120
	ds_read_b128 v[84:87], v240 offset:5136
	ds_read_b128 v[152:155], v240 offset:7680
	ds_read_b128 v[156:159], v240 offset:7696
	s_waitcnt lgkmcnt(4)
	v_mfma_scale_f32_32x32x64_f8f6f4 v[32:47], v[144:151], v[232:239], v[32:47], v207, v207 op_sel_hi:[0,0,0]
	v_max_f32_e32 v88, v96, v97
	v_max3_f32 v88, v88, v98, v99
	v_max3_f32 v88, v88, v100, v101
	v_max3_f32 v88, v88, v102, v103
	v_max3_f32 v88, v88, v104, v105
	v_max3_f32 v88, v88, v106, v107
	s_waitcnt lgkmcnt(2)
	v_mfma_scale_f32_32x32x64_f8f6f4 v[16:31], v[144:151], v[80:87], v[16:31], v207, v207 op_sel_hi:[0,0,0]
	v_max3_f32 v88, v88, v108, v109
	v_max3_f32 v88, v88, v110, v111
	v_mov_b32_e32 v89, v88
	s_nop 1
	v_permlane32_swap_b32_e32 v88, v89
	v_max_f32_e32 v80, v88, v89
	v_fma_f32 v81, v80, s38, -v176
	v_cmp_ge_f32_e32 vcc, s68, v81
	v_fmamk_f32 v80, v80, 0x3dd53b94, v204
	v_max_f32_e32 v80, v176, v80
	v_sub_f32_e32 v81, v176, v80
	v_exp_f32_e32 v81, v81
	s_waitcnt lgkmcnt(0)
	v_mfma_scale_f32_32x32x64_f8f6f4 v[0:15], v[144:151], v[152:159], v[0:15], v207, v207 op_sel_hi:[0,0,0]
	s_cmp_eq_u64 vcc, exec
	s_cselect_b64 vcc, -1, 0
	v_cndmask_b32_e32 v194, v80, v176, vcc
	v_fma_f32 v178, v96, s38, -v194
	v_fma_f32 v179, v97, s38, -v194
	v_fma_f32 v176, v98, s38, -v194
	v_fma_f32 v177, v99, s38, -v194
	v_fma_f32 v162, v100, s38, -v194
	v_fma_f32 v163, v101, s38, -v194
	v_fma_f32 v160, v102, s38, -v194
	v_fma_f32 v161, v103, s38, -v194
	v_fma_f32 v158, v104, s38, -v194
	v_fma_f32 v159, v105, s38, -v194
	v_fma_f32 v156, v106, s38, -v194
	v_fma_f32 v157, v107, s38, -v194
	v_fma_f32 v154, v108, s38, -v194
	v_fma_f32 v155, v109, s38, -v194
	v_fma_f32 v152, v110, s38, -v194
	v_fma_f32 v153, v111, s38, -v194
	v_cndmask_b32_e64 v88, v81, 1.0, vcc
	s_add_i32 s17, s17, 2
	s_add_i32 s76, s76, 1
	s_and_b64 vcc, exec, s[18:19]
	v_mfma_scale_f32_32x32x64_f8f6f4 v[64:79], v[144:151], v[112:119], v[64:79], v207, v207 op_sel_hi:[0,0,0]
	s_barrier
	s_cbranch_vccnz .LBB0_1889
